# small in-proj columns (gates, indexer keys) moved out of the 256-wide tile round into a K-split skinny MFMA pass over all CUs with LDS tree reduction; plus rewritten index scoring loop
# speedup vs baseline: 1.0139x; 1.0139x over previous
.LBB0_146:
	s_mul_i32 s0, s1, 10
	v_writelane_b32 v254, s0, 36
	s_or_b32 s4, s0, 1
	s_lshr_b32 s0, s1, 1
	v_writelane_b32 v254, s0, 37
	s_and_b32 s0, s1, 1
	s_cmp_eq_u32 s0, 0
	v_writelane_b32 v254, s1, 38
	s_cselect_b64 s[6:7], -1, 0
	s_cmp_eq_u32 s0, 1
	v_writelane_b32 v254, s0, 39
	s_cselect_b64 s[0:1], -1, 0
	s_cmp_le_i32 s94, s4
	s_mov_b64 s[12:13], s[92:93]
	s_cselect_b64 s[8:9], -1, 0
	s_cmp_lt_i32 s4, s95
	s_cselect_b64 s[10:11], -1, 0
	s_and_b64 s[8:9], s[8:9], s[10:11]
	v_writelane_b32 v254, s12, 40
	s_andn2_b64 vcc, exec, s[8:9]
	s_nop 0
	v_writelane_b32 v254, s13, 41
	s_cbranch_vccnz .LBB0_227
	s_and_b64 s[8:9], s[6:7], exec
	s_movk_i32 s4, 0x1900
	s_cselect_b32 s44, s4, 0x1100
	v_readlane_b32 s4, v253, 0
	s_lshr_b32 s10, s44, 2
	s_sub_i32 s10, s10, 64
	s_waitcnt vmcnt(0)
	v_mbcnt_lo_u32_b32 v8, -1, 0
	v_mbcnt_hi_u32_b32 v8, -1, v8
	s_cmp_ge_i32 s2, s10
	v_lshl_add_u32 v0, s4, 6, v8
	s_nop 0
	v_readfirstlane_b32 s45, v0
	s_cbranch_scc1 .LBB0_175
	v_lshlrev_b32_e32 v1, 4, v0
	v_add_u32_e32 v2, 0x2000, v1
	v_ashrrev_i32_e32 v3, 31, v2
	v_lshrrev_b32_e32 v3, 22, v3
	v_add_u32_e32 v3, v2, v3
	v_ashrrev_i32_e32 v9, 10, v3
	v_mul_i32_i24_e32 v3, 0x400, v9
	v_readlane_b32 s8, v254, 40
	v_sub_u32_e32 v2, v2, v3
	v_readlane_b32 s9, v254, 41
	s_add_u32 s46, s8, 0x1f600000
	v_lshrrev_b32_e32 v3, 4, v2
	s_addc_u32 s47, s9, 0
	v_bitop3_b32 v2, v3, v2, 32 bitop3:0x6c
	s_and_b64 s[6:7], s[6:7], exec
	v_ashrrev_i32_e32 v3, 31, v2
	s_cselect_b32 s4, s73, 0x3400000
	v_lshrrev_b32_e32 v3, 26, v3
	s_add_u32 s8, s8, s4
	v_readlane_b32 s4, v254, 37
	v_add_u32_e32 v3, v2, v3
	v_lshlrev_b32_e32 v4, 3, v9
	s_mul_i32 s4, s4, s44
	v_ashrrev_i32_e32 v10, 6, v3
	v_and_b32_e32 v4, -16, v4
	s_addc_u32 s9, s9, 0
	s_lshl_b32 s4, s4, 11
	v_add_u32_e32 v4, v10, v4
	s_lshl_b64 s[6:7], s[4:5], 1
	v_and_b32_e32 v5, 3, v10
	s_mov_b32 s4, 0xfffe0
	v_lshrrev_b32_e32 v6, 2, v4
	v_lshlrev_b32_e32 v7, 1, v4
	v_and_b32_e32 v3, 0xc0, v3
	v_and_or_b32 v5, v4, s4, v5
	v_and_b32_e32 v6, 4, v6
	v_and_b32_e32 v7, 24, v7
	v_sub_u32_e32 v2, v2, v3
	v_or3_b32 v5, v5, v6, v7
	v_lshlrev_b32_e32 v6, 5, v9
	v_ashrrev_i16_sdwa v2, v187, sext(v2) dst_sel:DWORD dst_unused:UNUSED_PAD src0_sel:DWORD src1_sel:BYTE_0
	v_and_b32_e32 v6, 32, v6
	v_bfe_i32 v11, v2, 0, 16
	v_add_lshl_u32 v2, v6, v11, 1
	v_lshl_add_u32 v128, v5, 12, v2
	v_lshl_add_u32 v130, v4, 12, v2
	v_bfe_i32 v2, v0, 27, 1
	v_lshrrev_b32_e32 v2, 22, v2
	v_add_u32_e32 v2, v1, v2
	v_and_b32_e32 v2, 0xfffffc00, v2
	v_sub_u32_e32 v1, v1, v2
	v_lshrrev_b32_e32 v2, 4, v1
	v_ashrrev_i32_e32 v3, 31, v0
	v_bitop3_b32 v1, v2, v1, 32 bitop3:0x6c
	v_lshrrev_b32_e32 v3, 26, v3
	v_ashrrev_i32_e32 v2, 31, v1
	v_add_u32_e32 v0, v0, v3
	v_lshrrev_b32_e32 v2, 26, v2
	v_ashrrev_i32_e32 v13, 6, v0
	v_add_u32_e32 v2, v1, v2
	v_lshlrev_b32_e32 v0, 3, v13
	s_add_u32 s48, s8, s6
	v_ashrrev_i32_e32 v12, 6, v2
	v_and_b32_e32 v0, -16, v0
	s_addc_u32 s49, s9, s7
	s_lshr_b32 s50, s44, 5
	s_sub_i32 s50, s50, 8
	v_add_u32_e32 v0, v12, v0
	v_and_b32_e32 v3, 3, v12
	v_lshrrev_b32_e32 v4, 2, v0
	v_lshlrev_b32_e32 v5, 1, v0
	v_and_b32_e32 v2, 0xc0, v2
	s_abs_i32 s52, s50
	v_and_or_b32 v3, v0, s4, v3
	v_and_b32_e32 v4, 4, v4
	v_and_b32_e32 v5, 24, v5
	v_sub_u32_e32 v1, v1, v2
	v_cvt_f32_u32_e32 v2, s52
	v_or3_b32 v3, v3, v4, v5
	v_lshlrev_b32_e32 v4, 5, v13
	v_ashrrev_i16_sdwa v1, v187, sext(v1) dst_sel:DWORD dst_unused:UNUSED_PAD src0_sel:DWORD src1_sel:BYTE_0
	v_and_b32_e32 v4, 32, v4
	v_bfe_i32 v14, v1, 0, 16
	v_add_lshl_u32 v1, v4, v14, 1
	v_lshl_add_u32 v132, v0, 12, v1
	v_rcp_iflag_f32_e32 v0, v2
	v_readlane_b32 s4, v253, 47
	s_or_b32 s4, s50, s4
	v_readlane_b32 s6, v253, 48
	v_mul_f32_e32 v0, 0x4f7ffffe, v0
	v_cvt_u32_f32_e32 v0, v0
	s_sub_i32 s11, 0, s52
	s_mul_i32 s4, s4, s6
	v_readlane_b32 s6, v254, 24
	v_readfirstlane_b32 s54, v0
	s_mul_i32 s11, s11, s54
	v_readlane_b32 s7, v254, 25
	s_add_i32 s4, s4, s6
	s_mul_hi_u32 s11, s54, s11
	s_abs_i32 s7, s4
	s_add_i32 s54, s54, s11
	s_mul_hi_u32 s11, s7, s54
	s_mul_i32 s12, s11, s52
	s_ashr_i32 s8, s45, 6
	s_ashr_i32 s6, s4, 31
	s_ashr_i32 s53, s50, 31
	s_sub_i32 s7, s7, s12
	s_ashr_i32 s9, s45, 8
	s_lshl_b32 s51, s8, 10
	s_xor_b32 s6, s6, s53
	s_add_i32 s12, s11, 1
	s_sub_i32 s13, s7, s52
	s_cmp_ge_u32 s7, s52
	s_cselect_b32 s11, s12, s11
	s_cselect_b32 s7, s13, s7
	s_add_i32 s12, s11, 1
	s_cmp_ge_u32 s7, s52
	s_cselect_b32 s7, s12, s11
	s_xor_b32 s7, s7, s6
	s_sub_i32 s6, s7, s6
	s_lshl_b32 s11, s6, 3
	s_sub_i32 s7, 64, s11
	s_min_i32 s12, s7, 8
	s_sext_i32_i16 s7, s12
	v_cvt_f32_i32_e32 v0, s7
	s_mul_i32 s6, s6, s50
	s_sub_i32 s13, s4, s6
	v_lshl_add_u32 v136, v3, 12, v1
	v_cvt_f32_i32_e32 v1, s13
	v_rcp_iflag_f32_e32 v2, v0
	s_xor_b32 s4, s13, s7
	s_ashr_i32 s4, s4, 30
	s_or_b32 s4, s4, 1
	v_mul_f32_e32 v2, v1, v2
	v_trunc_f32_e32 v2, v2
	v_fma_f32 v1, -v2, v0, v1
	v_cvt_i32_f32_e32 v2, v2
	v_cmp_ge_f32_e64 s[6:7], |v1|, |v0|
	s_and_b64 s[6:7], s[6:7], exec
	s_cselect_b32 s4, s4, 0
	v_readfirstlane_b32 s6, v2
	s_add_i32 s4, s6, s4
	s_mul_i32 s6, s4, s12
	s_sub_i32 s6, s13, s6
	s_sext_i32_i16 s6, s6
	s_add_i32 s30, s11, s6
	s_ashr_i32 s31, s30, 31
	s_bfe_i64 s[12:13], s[4:5], 0x100000
	s_lshl_b64 s[6:7], s[30:31], 20
	s_lshl_b64 s[12:13], s[12:13], 20
	s_add_u32 s40, s48, s12
	s_addc_u32 s41, s49, s13
	s_add_i32 s21, s51, 0
	s_add_i32 m0, s21, 0x10000
	v_mov_b32_e32 v129, v137
	global_load_lds_dwordx4 v136, s[40:41]
	s_add_i32 m0, s21, 0x12000
	s_add_u32 s38, s46, s6
	global_load_lds_dwordx4 v128, s[40:41]
	s_addc_u32 s39, s47, s7
	s_mov_b32 m0, s21
	s_add_i32 s55, s21, 0x2000
	global_load_lds_dwordx4 v132, s[38:39]
	s_mov_b32 m0, s55
	s_add_u32 s6, s40, 0x80000
	global_load_lds_dwordx4 v130, s[38:39]
	s_addc_u32 s7, s41, 0
	s_add_i32 m0, s21, 0x14000
	v_mov_b32_e32 v133, v137
	global_load_lds_dwordx4 v136, s[6:7]
	s_add_i32 m0, s21, 0x16000
	v_mov_b32_e32 v131, v137
	global_load_lds_dwordx4 v128, s[6:7]
	s_add_u32 s6, s38, 0x80000
	s_addc_u32 s7, s39, 0
	s_add_i32 s56, s21, 0x4000
	s_mov_b32 m0, s56
	s_add_i32 s57, s21, 0x6000
	global_load_lds_dwordx4 v132, s[6:7]
	s_mov_b32 m0, s57
	v_lshl_add_u64 v[6:7], s[40:41], 0, v[136:137]
	global_load_lds_dwordx4 v130, s[6:7]
	v_readlane_b32 s6, v253, 3
	v_readlane_b32 s7, v253, 4
	s_load_dword s58, s[6:7], 0x0
	v_lshl_add_u64 v[4:5], s[40:41], 0, v[128:129]
	v_lshl_add_u64 v[2:3], s[38:39], 0, v[132:133]
	s_cmp_lg_u32 s9, 1
	v_lshl_add_u64 v[0:1], s[38:39], 0, v[130:131]
	s_cbranch_scc1 .LBB0_150
	s_barrier

.LBB0_174:
	s_barrier
	v_readlane_b32 s6, v253, 0
	v_readlane_b32 s8, v254, 40
	v_readlane_b32 s9, v254, 41
	v_readlane_b32 s7, v254, 39
	v_readlane_b32 s10, v254, 37
	s_load_dword s63, s[90:91], 0xc8
	v_mbcnt_lo_u32_b32 v206, -1, 0
	v_mbcnt_hi_u32_b32 v206, -1, v206
	s_movk_i32 s11, 0x1100
	s_mov_b32 s14, 0x3400000
	s_cmp_eq_u32 s7, 0
	s_cselect_b32 s11, 0x1900, s11
	s_cselect_b32 s14, 0x200000, s14
	s_mul_i32 s13, s10, s11
	s_add_i32 s13, s13, s11
	s_addk_i32 s13, 0xff00
	s_lshl_b32 s13, s13, 12
	s_add_u32 s14, s14, s13
	v_lshlrev_b32_e32 v207, 4, v206
	v_and_b32_e32 v209, 15, v206
	v_lshrrev_b32_e32 v210, 4, v206
	v_lshlrev_b32_e32 v210, 4, v210
	s_and_b32 s13, s6, 3
	s_mul_i32 s13, s13, 0x5000
	v_add_u32_e32 v207, s13, v207
	v_lshl_or_b32 v208, v209, 9, v210
	v_lshl_or_b32 v206, v209, 12, v210
	s_mov_b32 s64, s2
	s_waitcnt lgkmcnt(0)
.Lsk2_loop:
	s_cmp_eq_u32 s7, 0
	s_cbranch_scc0 .Lsk2_odd
	s_lshl_b32 s60, s64, 18
	s_lshl_b32 s61, s6, 9
	s_add_u32 s60, s60, s61
	s_add_u32 s60, s60, 0x1f600000
	s_add_u32 s42, s8, s60
	s_addc_u32 s43, s9, 0
	s_add_u32 s44, s42, 0x10000
	s_addc_u32 s45, s43, 0
	s_add_u32 s46, s44, 0x10000
	s_addc_u32 s47, s45, 0
	s_add_u32 s48, s46, 0x10000
	s_addc_u32 s49, s47, 0
	s_add_u32 s60, s14, s61
	s_add_u32 s50, s8, s60
	s_addc_u32 s51, s9, 0
	s_add_u32 s52, s50, 0x10000
	s_addc_u32 s53, s51, 0
	v_mov_b32_e32 v108, 0
	v_mov_b32_e32 v109, 0
	v_mov_b32_e32 v110, 0
	v_mov_b32_e32 v111, 0
	v_mov_b32_e32 v112, 0
	v_mov_b32_e32 v113, 0
	v_mov_b32_e32 v114, 0
	v_mov_b32_e32 v115, 0
	v_mov_b32_e32 v116, 0
	v_mov_b32_e32 v117, 0
	v_mov_b32_e32 v118, 0
	v_mov_b32_e32 v119, 0
	v_mov_b32_e32 v120, 0
	v_mov_b32_e32 v121, 0
	v_mov_b32_e32 v122, 0
	v_mov_b32_e32 v123, 0
	v_mov_b32_e32 v124, 0
	v_mov_b32_e32 v125, 0
	v_mov_b32_e32 v126, 0
	v_mov_b32_e32 v127, 0
	v_mov_b32_e32 v146, 0
	v_mov_b32_e32 v147, 0
	v_mov_b32_e32 v148, 0
	v_mov_b32_e32 v149, 0
	v_mov_b32_e32 v150, 0
	v_mov_b32_e32 v151, 0
	v_mov_b32_e32 v152, 0
	v_mov_b32_e32 v153, 0
	v_mov_b32_e32 v154, 0
	v_mov_b32_e32 v155, 0
	v_mov_b32_e32 v156, 0
	v_mov_b32_e32 v157, 0
	global_load_dwordx4 v[0:3], v206, s[42:43]
	global_load_dwordx4 v[4:7], v206, s[44:45]
	global_load_dwordx4 v[8:11], v206, s[46:47]
	global_load_dwordx4 v[12:15], v206, s[48:49]
	global_load_dwordx4 v[16:19], v206, s[50:51]
	global_load_dwordx4 v[20:23], v206, s[52:53]
	global_load_dwordx4 v[36:39], v206, s[42:43] offset:64
	global_load_dwordx4 v[40:43], v206, s[44:45] offset:64
	global_load_dwordx4 v[44:47], v206, s[46:47] offset:64
	global_load_dwordx4 v[48:51], v206, s[48:49] offset:64
	global_load_dwordx4 v[52:55], v206, s[50:51] offset:64
	global_load_dwordx4 v[56:59], v206, s[52:53] offset:64
	global_load_dwordx4 v[72:75], v206, s[42:43] offset:128
	global_load_dwordx4 v[76:79], v206, s[44:45] offset:128
	global_load_dwordx4 v[80:83], v206, s[46:47] offset:128
	global_load_dwordx4 v[84:87], v206, s[48:49] offset:128
	global_load_dwordx4 v[88:91], v206, s[50:51] offset:128
	global_load_dwordx4 v[92:95], v206, s[52:53] offset:128
	s_waitcnt vmcnt(12)
	v_mfma_f32_16x16x32_bf16 v[108:111], v[16:19], v[0:3], v[108:111]
	v_mfma_f32_16x16x32_bf16 v[112:115], v[20:23], v[0:3], v[112:115]
	v_mfma_f32_16x16x32_bf16 v[116:119], v[16:19], v[4:7], v[116:119]
	v_mfma_f32_16x16x32_bf16 v[120:123], v[20:23], v[4:7], v[120:123]
	v_mfma_f32_16x16x32_bf16 v[124:127], v[16:19], v[8:11], v[124:127]
	v_mfma_f32_16x16x32_bf16 v[146:149], v[20:23], v[8:11], v[146:149]
	v_mfma_f32_16x16x32_bf16 v[150:153], v[16:19], v[12:15], v[150:153]
	v_mfma_f32_16x16x32_bf16 v[154:157], v[20:23], v[12:15], v[154:157]
	global_load_dwordx4 v[0:3], v206, s[42:43] offset:192
	global_load_dwordx4 v[4:7], v206, s[44:45] offset:192
	global_load_dwordx4 v[8:11], v206, s[46:47] offset:192
	global_load_dwordx4 v[12:15], v206, s[48:49] offset:192
	global_load_dwordx4 v[16:19], v206, s[50:51] offset:192
	global_load_dwordx4 v[20:23], v206, s[52:53] offset:192
	s_waitcnt vmcnt(12)
	v_mfma_f32_16x16x32_bf16 v[108:111], v[52:55], v[36:39], v[108:111]
	v_mfma_f32_16x16x32_bf16 v[112:115], v[56:59], v[36:39], v[112:115]
	v_mfma_f32_16x16x32_bf16 v[116:119], v[52:55], v[40:43], v[116:119]
	v_mfma_f32_16x16x32_bf16 v[120:123], v[56:59], v[40:43], v[120:123]
	v_mfma_f32_16x16x32_bf16 v[124:127], v[52:55], v[44:47], v[124:127]
	v_mfma_f32_16x16x32_bf16 v[146:149], v[56:59], v[44:47], v[146:149]
	v_mfma_f32_16x16x32_bf16 v[150:153], v[52:55], v[48:51], v[150:153]
	v_mfma_f32_16x16x32_bf16 v[154:157], v[56:59], v[48:51], v[154:157]
	global_load_dwordx4 v[36:39], v206, s[42:43] offset:256
	global_load_dwordx4 v[40:43], v206, s[44:45] offset:256
	global_load_dwordx4 v[44:47], v206, s[46:47] offset:256
	global_load_dwordx4 v[48:51], v206, s[48:49] offset:256
	global_load_dwordx4 v[52:55], v206, s[50:51] offset:256
	global_load_dwordx4 v[56:59], v206, s[52:53] offset:256
	s_waitcnt vmcnt(12)
	v_mfma_f32_16x16x32_bf16 v[108:111], v[88:91], v[72:75], v[108:111]
	v_mfma_f32_16x16x32_bf16 v[112:115], v[92:95], v[72:75], v[112:115]
	v_mfma_f32_16x16x32_bf16 v[116:119], v[88:91], v[76:79], v[116:119]
	v_mfma_f32_16x16x32_bf16 v[120:123], v[92:95], v[76:79], v[120:123]
	v_mfma_f32_16x16x32_bf16 v[124:127], v[88:91], v[80:83], v[124:127]
	v_mfma_f32_16x16x32_bf16 v[146:149], v[92:95], v[80:83], v[146:149]
	v_mfma_f32_16x16x32_bf16 v[150:153], v[88:91], v[84:87], v[150:153]
	v_mfma_f32_16x16x32_bf16 v[154:157], v[92:95], v[84:87], v[154:157]
	global_load_dwordx4 v[72:75], v206, s[42:43] offset:320
	global_load_dwordx4 v[76:79], v206, s[44:45] offset:320
	global_load_dwordx4 v[80:83], v206, s[46:47] offset:320
	global_load_dwordx4 v[84:87], v206, s[48:49] offset:320
	global_load_dwordx4 v[88:91], v206, s[50:51] offset:320
	global_load_dwordx4 v[92:95], v206, s[52:53] offset:320
	s_waitcnt vmcnt(12)
	v_mfma_f32_16x16x32_bf16 v[108:111], v[16:19], v[0:3], v[108:111]
	v_mfma_f32_16x16x32_bf16 v[112:115], v[20:23], v[0:3], v[112:115]
	v_mfma_f32_16x16x32_bf16 v[116:119], v[16:19], v[4:7], v[116:119]
	v_mfma_f32_16x16x32_bf16 v[120:123], v[20:23], v[4:7], v[120:123]
	v_mfma_f32_16x16x32_bf16 v[124:127], v[16:19], v[8:11], v[124:127]
	v_mfma_f32_16x16x32_bf16 v[146:149], v[20:23], v[8:11], v[146:149]
	v_mfma_f32_16x16x32_bf16 v[150:153], v[16:19], v[12:15], v[150:153]
	v_mfma_f32_16x16x32_bf16 v[154:157], v[20:23], v[12:15], v[154:157]
	global_load_dwordx4 v[0:3], v206, s[42:43] offset:384
	global_load_dwordx4 v[4:7], v206, s[44:45] offset:384
	global_load_dwordx4 v[8:11], v206, s[46:47] offset:384
	global_load_dwordx4 v[12:15], v206, s[48:49] offset:384
	global_load_dwordx4 v[16:19], v206, s[50:51] offset:384
	global_load_dwordx4 v[20:23], v206, s[52:53] offset:384
	s_waitcnt vmcnt(12)
	v_mfma_f32_16x16x32_bf16 v[108:111], v[52:55], v[36:39], v[108:111]
	v_mfma_f32_16x16x32_bf16 v[112:115], v[56:59], v[36:39], v[112:115]
	v_mfma_f32_16x16x32_bf16 v[116:119], v[52:55], v[40:43], v[116:119]
	v_mfma_f32_16x16x32_bf16 v[120:123], v[56:59], v[40:43], v[120:123]
	v_mfma_f32_16x16x32_bf16 v[124:127], v[52:55], v[44:47], v[124:127]
	v_mfma_f32_16x16x32_bf16 v[146:149], v[56:59], v[44:47], v[146:149]
	v_mfma_f32_16x16x32_bf16 v[150:153], v[52:55], v[48:51], v[150:153]
	v_mfma_f32_16x16x32_bf16 v[154:157], v[56:59], v[48:51], v[154:157]
	global_load_dwordx4 v[36:39], v206, s[42:43] offset:448
	global_load_dwordx4 v[40:43], v206, s[44:45] offset:448
	global_load_dwordx4 v[44:47], v206, s[46:47] offset:448
	global_load_dwordx4 v[48:51], v206, s[48:49] offset:448
	global_load_dwordx4 v[52:55], v206, s[50:51] offset:448
	global_load_dwordx4 v[56:59], v206, s[52:53] offset:448
	s_waitcnt vmcnt(12)
	v_mfma_f32_16x16x32_bf16 v[108:111], v[88:91], v[72:75], v[108:111]
	v_mfma_f32_16x16x32_bf16 v[112:115], v[92:95], v[72:75], v[112:115]
	v_mfma_f32_16x16x32_bf16 v[116:119], v[88:91], v[76:79], v[116:119]
	v_mfma_f32_16x16x32_bf16 v[120:123], v[92:95], v[76:79], v[120:123]
	v_mfma_f32_16x16x32_bf16 v[124:127], v[88:91], v[80:83], v[124:127]
	v_mfma_f32_16x16x32_bf16 v[146:149], v[92:95], v[80:83], v[146:149]
	v_mfma_f32_16x16x32_bf16 v[150:153], v[88:91], v[84:87], v[150:153]
	v_mfma_f32_16x16x32_bf16 v[154:157], v[92:95], v[84:87], v[154:157]
	s_waitcnt vmcnt(6)
	v_mfma_f32_16x16x32_bf16 v[108:111], v[16:19], v[0:3], v[108:111]
	v_mfma_f32_16x16x32_bf16 v[112:115], v[20:23], v[0:3], v[112:115]
	v_mfma_f32_16x16x32_bf16 v[116:119], v[16:19], v[4:7], v[116:119]
	v_mfma_f32_16x16x32_bf16 v[120:123], v[20:23], v[4:7], v[120:123]
	v_mfma_f32_16x16x32_bf16 v[124:127], v[16:19], v[8:11], v[124:127]
	v_mfma_f32_16x16x32_bf16 v[146:149], v[20:23], v[8:11], v[146:149]
	v_mfma_f32_16x16x32_bf16 v[150:153], v[16:19], v[12:15], v[150:153]
	v_mfma_f32_16x16x32_bf16 v[154:157], v[20:23], v[12:15], v[154:157]
	s_waitcnt vmcnt(0)
	v_mfma_f32_16x16x32_bf16 v[108:111], v[52:55], v[36:39], v[108:111]
	v_mfma_f32_16x16x32_bf16 v[112:115], v[56:59], v[36:39], v[112:115]
	v_mfma_f32_16x16x32_bf16 v[116:119], v[52:55], v[40:43], v[116:119]
	v_mfma_f32_16x16x32_bf16 v[120:123], v[56:59], v[40:43], v[120:123]
	v_mfma_f32_16x16x32_bf16 v[124:127], v[52:55], v[44:47], v[124:127]
	v_mfma_f32_16x16x32_bf16 v[146:149], v[56:59], v[44:47], v[146:149]
	v_mfma_f32_16x16x32_bf16 v[150:153], v[52:55], v[48:51], v[150:153]
	v_mfma_f32_16x16x32_bf16 v[154:157], v[56:59], v[48:51], v[154:157]
	s_nop 7
	s_nop 1
	s_cmp_lt_u32 s6, 4
	s_cbranch_scc1 .Lsk2e_a1
	ds_write_b128 v207, v[108:111] offset:0
	ds_write_b128 v207, v[112:115] offset:1024
	ds_write_b128 v207, v[116:119] offset:2048
	ds_write_b128 v207, v[120:123] offset:3072
	ds_write_b128 v207, v[124:127] offset:4096
	ds_write_b128 v207, v[146:149] offset:5120
	ds_write_b128 v207, v[150:153] offset:6144
	ds_write_b128 v207, v[154:157] offset:7168
	s_waitcnt lgkmcnt(0)
.Lsk2e_a1:
	s_barrier
	s_cmp_lt_u32 s6, 4
	s_cbranch_scc0 .Lsk2e_a2
	ds_read_b128 v[0:3], v207 offset:0
	ds_read_b128 v[4:7], v207 offset:1024
	ds_read_b128 v[8:11], v207 offset:2048
	ds_read_b128 v[12:15], v207 offset:3072
	ds_read_b128 v[16:19], v207 offset:4096
	ds_read_b128 v[20:23], v207 offset:5120
	ds_read_b128 v[24:27], v207 offset:6144
	ds_read_b128 v[28:31], v207 offset:7168
	s_waitcnt lgkmcnt(0)
	v_add_f32_e32 v108, v108, v0
	v_add_f32_e32 v109, v109, v1
	v_add_f32_e32 v110, v110, v2
	v_add_f32_e32 v111, v111, v3
	v_add_f32_e32 v112, v112, v4
	v_add_f32_e32 v113, v113, v5
	v_add_f32_e32 v114, v114, v6
	v_add_f32_e32 v115, v115, v7
	v_add_f32_e32 v116, v116, v8
	v_add_f32_e32 v117, v117, v9
	v_add_f32_e32 v118, v118, v10
	v_add_f32_e32 v119, v119, v11
	v_add_f32_e32 v120, v120, v12
	v_add_f32_e32 v121, v121, v13
	v_add_f32_e32 v122, v122, v14
	v_add_f32_e32 v123, v123, v15
	v_add_f32_e32 v124, v124, v16
	v_add_f32_e32 v125, v125, v17
	v_add_f32_e32 v126, v126, v18
	v_add_f32_e32 v127, v127, v19
	v_add_f32_e32 v146, v146, v20
	v_add_f32_e32 v147, v147, v21
	v_add_f32_e32 v148, v148, v22
	v_add_f32_e32 v149, v149, v23
	v_add_f32_e32 v150, v150, v24
	v_add_f32_e32 v151, v151, v25
	v_add_f32_e32 v152, v152, v26
	v_add_f32_e32 v153, v153, v27
	v_add_f32_e32 v154, v154, v28
	v_add_f32_e32 v155, v155, v29
	v_add_f32_e32 v156, v156, v30
	v_add_f32_e32 v157, v157, v31
.Lsk2e_a2:
	s_barrier
	s_cmp_lt_u32 s6, 4
	s_cbranch_scc0 .Lsk2e_b1
	s_cmp_lt_u32 s6, 2
	s_cbranch_scc1 .Lsk2e_b1
	ds_write_b128 v207, v[108:111] offset:0
	ds_write_b128 v207, v[112:115] offset:1024
	ds_write_b128 v207, v[116:119] offset:2048
	ds_write_b128 v207, v[120:123] offset:3072
	ds_write_b128 v207, v[124:127] offset:4096
	ds_write_b128 v207, v[146:149] offset:5120
	ds_write_b128 v207, v[150:153] offset:6144
	ds_write_b128 v207, v[154:157] offset:7168
	s_waitcnt lgkmcnt(0)
.Lsk2e_b1:
	s_barrier
	s_cmp_lt_u32 s6, 2
	s_cbranch_scc0 .Lsk2e_b2
	v_add_u32_e32 v207, 0xa000, v207
	ds_read_b128 v[0:3], v207 offset:0
	ds_read_b128 v[4:7], v207 offset:1024
	ds_read_b128 v[8:11], v207 offset:2048
	ds_read_b128 v[12:15], v207 offset:3072
	ds_read_b128 v[16:19], v207 offset:4096
	ds_read_b128 v[20:23], v207 offset:5120
	ds_read_b128 v[24:27], v207 offset:6144
	ds_read_b128 v[28:31], v207 offset:7168
	s_waitcnt lgkmcnt(0)
	v_add_f32_e32 v108, v108, v0
	v_add_f32_e32 v109, v109, v1
	v_add_f32_e32 v110, v110, v2
	v_add_f32_e32 v111, v111, v3
	v_add_f32_e32 v112, v112, v4
	v_add_f32_e32 v113, v113, v5
	v_add_f32_e32 v114, v114, v6
	v_add_f32_e32 v115, v115, v7
	v_add_f32_e32 v116, v116, v8
	v_add_f32_e32 v117, v117, v9
	v_add_f32_e32 v118, v118, v10
	v_add_f32_e32 v119, v119, v11
	v_add_f32_e32 v120, v120, v12
	v_add_f32_e32 v121, v121, v13
	v_add_f32_e32 v122, v122, v14
	v_add_f32_e32 v123, v123, v15
	v_add_f32_e32 v124, v124, v16
	v_add_f32_e32 v125, v125, v17
	v_add_f32_e32 v126, v126, v18
	v_add_f32_e32 v127, v127, v19
	v_add_f32_e32 v146, v146, v20
	v_add_f32_e32 v147, v147, v21
	v_add_f32_e32 v148, v148, v22
	v_add_f32_e32 v149, v149, v23
	v_add_f32_e32 v150, v150, v24
	v_add_f32_e32 v151, v151, v25
	v_add_f32_e32 v152, v152, v26
	v_add_f32_e32 v153, v153, v27
	v_add_f32_e32 v154, v154, v28
	v_add_f32_e32 v155, v155, v29
	v_add_f32_e32 v156, v156, v30
	v_add_f32_e32 v157, v157, v31
	v_add_u32_e32 v207, 0xffff6000, v207
.Lsk2e_b2:
	s_barrier
	s_cmp_eq_u32 s6, 1
	s_cbranch_scc0 .Lsk2e_c1
	ds_write_b128 v207, v[108:111] offset:0
	ds_write_b128 v207, v[112:115] offset:1024
	ds_write_b128 v207, v[116:119] offset:2048
	ds_write_b128 v207, v[120:123] offset:3072
	ds_write_b128 v207, v[124:127] offset:4096
	ds_write_b128 v207, v[146:149] offset:5120
	ds_write_b128 v207, v[150:153] offset:6144
	ds_write_b128 v207, v[154:157] offset:7168
	s_waitcnt lgkmcnt(0)
.Lsk2e_c1:
	s_barrier
	s_cmp_eq_u32 s6, 0
	s_cbranch_scc0 .Lsk2e_c2
	v_add_u32_e32 v207, 0x5000, v207
	ds_read_b128 v[0:3], v207 offset:0
	ds_read_b128 v[4:7], v207 offset:1024
	ds_read_b128 v[8:11], v207 offset:2048
	ds_read_b128 v[12:15], v207 offset:3072
	ds_read_b128 v[16:19], v207 offset:4096
	ds_read_b128 v[20:23], v207 offset:5120
	ds_read_b128 v[24:27], v207 offset:6144
	ds_read_b128 v[28:31], v207 offset:7168
	s_waitcnt lgkmcnt(0)
	v_add_f32_e32 v108, v108, v0
	v_add_f32_e32 v109, v109, v1
	v_add_f32_e32 v110, v110, v2
	v_add_f32_e32 v111, v111, v3
	v_add_f32_e32 v112, v112, v4
	v_add_f32_e32 v113, v113, v5
	v_add_f32_e32 v114, v114, v6
	v_add_f32_e32 v115, v115, v7
	v_add_f32_e32 v116, v116, v8
	v_add_f32_e32 v117, v117, v9
	v_add_f32_e32 v118, v118, v10
	v_add_f32_e32 v119, v119, v11
	v_add_f32_e32 v120, v120, v12
	v_add_f32_e32 v121, v121, v13
	v_add_f32_e32 v122, v122, v14
	v_add_f32_e32 v123, v123, v15
	v_add_f32_e32 v124, v124, v16
	v_add_f32_e32 v125, v125, v17
	v_add_f32_e32 v126, v126, v18
	v_add_f32_e32 v127, v127, v19
	v_add_f32_e32 v146, v146, v20
	v_add_f32_e32 v147, v147, v21
	v_add_f32_e32 v148, v148, v22
	v_add_f32_e32 v149, v149, v23
	v_add_f32_e32 v150, v150, v24
	v_add_f32_e32 v151, v151, v25
	v_add_f32_e32 v152, v152, v26
	v_add_f32_e32 v153, v153, v27
	v_add_f32_e32 v154, v154, v28
	v_add_f32_e32 v155, v155, v29
	v_add_f32_e32 v156, v156, v30
	v_add_f32_e32 v157, v157, v31
	v_add_u32_e32 v207, 0xffffb000, v207
	s_lshl_b32 s60, s64, 15
	s_add_u32 s60, s60, 0x31200000
	s_add_u32 s60, s8, s60
	s_addc_u32 s61, s9, 0
	global_store_dwordx4 v208, v[108:111], s[60:61]
	global_store_dwordx4 v208, v[112:115], s[60:61] offset:64
	s_add_u32 s60, s60, 0x2000
	s_addc_u32 s61, s61, 0
	global_store_dwordx4 v208, v[116:119], s[60:61]
	global_store_dwordx4 v208, v[120:123], s[60:61] offset:64
	s_add_u32 s60, s60, 0x2000
	s_addc_u32 s61, s61, 0
	global_store_dwordx4 v208, v[124:127], s[60:61]
	global_store_dwordx4 v208, v[146:149], s[60:61] offset:64
	s_add_u32 s60, s60, 0x2000
	s_addc_u32 s61, s61, 0
	global_store_dwordx4 v208, v[150:153], s[60:61]
	global_store_dwordx4 v208, v[154:157], s[60:61] offset:64
.Lsk2e_c2:
	s_barrier
	s_branch .Lsk2_next
.Lsk2_odd:
	s_lshl_b32 s60, s64, 18
	s_lshl_b32 s61, s6, 9
	s_add_u32 s60, s60, s61
	s_add_u32 s60, s60, 0x1f600000
	s_add_u32 s42, s8, s60
	s_addc_u32 s43, s9, 0
	s_add_u32 s44, s42, 0x10000
	s_addc_u32 s45, s43, 0
	s_add_u32 s46, s44, 0x10000
	s_addc_u32 s47, s45, 0
	s_add_u32 s48, s46, 0x10000
	s_addc_u32 s49, s47, 0
	s_add_u32 s60, s14, s61
	s_add_u32 s50, s8, s60
	s_addc_u32 s51, s9, 0
	s_add_u32 s52, s50, 0x10000
	s_addc_u32 s53, s51, 0
	s_add_u32 s54, s52, 0x10000
	s_addc_u32 s55, s53, 0
	s_add_u32 s56, s54, 0x10000
	s_addc_u32 s57, s55, 0
	s_add_u32 s58, s56, 0x10000
	s_addc_u32 s59, s57, 0
	v_mov_b32_e32 v108, 0
	v_mov_b32_e32 v109, 0
	v_mov_b32_e32 v110, 0
	v_mov_b32_e32 v111, 0
	v_mov_b32_e32 v112, 0
	v_mov_b32_e32 v113, 0
	v_mov_b32_e32 v114, 0
	v_mov_b32_e32 v115, 0
	v_mov_b32_e32 v116, 0
	v_mov_b32_e32 v117, 0
	v_mov_b32_e32 v118, 0
	v_mov_b32_e32 v119, 0
	v_mov_b32_e32 v120, 0
	v_mov_b32_e32 v121, 0
	v_mov_b32_e32 v122, 0
	v_mov_b32_e32 v123, 0
	v_mov_b32_e32 v124, 0
	v_mov_b32_e32 v125, 0
	v_mov_b32_e32 v126, 0
	v_mov_b32_e32 v127, 0
	v_mov_b32_e32 v146, 0
	v_mov_b32_e32 v147, 0
	v_mov_b32_e32 v148, 0
	v_mov_b32_e32 v149, 0
	v_mov_b32_e32 v150, 0
	v_mov_b32_e32 v151, 0
	v_mov_b32_e32 v152, 0
	v_mov_b32_e32 v153, 0
	v_mov_b32_e32 v154, 0
	v_mov_b32_e32 v155, 0
	v_mov_b32_e32 v156, 0
	v_mov_b32_e32 v157, 0
	v_mov_b32_e32 v158, 0
	v_mov_b32_e32 v159, 0
	v_mov_b32_e32 v160, 0
	v_mov_b32_e32 v161, 0
	v_mov_b32_e32 v162, 0
	v_mov_b32_e32 v163, 0
	v_mov_b32_e32 v164, 0
	v_mov_b32_e32 v165, 0
	v_mov_b32_e32 v166, 0
	v_mov_b32_e32 v167, 0
	v_mov_b32_e32 v168, 0
	v_mov_b32_e32 v169, 0
	v_mov_b32_e32 v170, 0
	v_mov_b32_e32 v171, 0
	v_mov_b32_e32 v172, 0
	v_mov_b32_e32 v173, 0
	v_mov_b32_e32 v174, 0
	v_mov_b32_e32 v175, 0
	v_mov_b32_e32 v176, 0
	v_mov_b32_e32 v177, 0
	v_mov_b32_e32 v178, 0
	v_mov_b32_e32 v179, 0
	v_mov_b32_e32 v180, 0
	v_mov_b32_e32 v181, 0
	v_mov_b32_e32 v212, 0
	v_mov_b32_e32 v213, 0
	v_mov_b32_e32 v214, 0
	v_mov_b32_e32 v215, 0
	v_mov_b32_e32 v216, 0
	v_mov_b32_e32 v217, 0
	v_mov_b32_e32 v218, 0
	v_mov_b32_e32 v219, 0
	v_mov_b32_e32 v220, 0
	v_mov_b32_e32 v221, 0
	v_mov_b32_e32 v222, 0
	v_mov_b32_e32 v223, 0
	v_mov_b32_e32 v224, 0
	v_mov_b32_e32 v225, 0
	v_mov_b32_e32 v226, 0
	v_mov_b32_e32 v227, 0
	v_mov_b32_e32 v228, 0
	v_mov_b32_e32 v229, 0
	v_mov_b32_e32 v230, 0
	v_mov_b32_e32 v231, 0
	v_mov_b32_e32 v232, 0
	v_mov_b32_e32 v233, 0
	v_mov_b32_e32 v234, 0
	v_mov_b32_e32 v235, 0
	global_load_dwordx4 v[0:3], v206, s[42:43]
	global_load_dwordx4 v[4:7], v206, s[44:45]
	global_load_dwordx4 v[8:11], v206, s[46:47]
	global_load_dwordx4 v[12:15], v206, s[48:49]
	global_load_dwordx4 v[16:19], v206, s[50:51]
	global_load_dwordx4 v[20:23], v206, s[52:53]
	global_load_dwordx4 v[24:27], v206, s[54:55]
	global_load_dwordx4 v[28:31], v206, s[56:57]
	global_load_dwordx4 v[32:35], v206, s[58:59]
	global_load_dwordx4 v[36:39], v206, s[42:43] offset:64
	global_load_dwordx4 v[40:43], v206, s[44:45] offset:64
	global_load_dwordx4 v[44:47], v206, s[46:47] offset:64
	global_load_dwordx4 v[48:51], v206, s[48:49] offset:64
	global_load_dwordx4 v[52:55], v206, s[50:51] offset:64
	global_load_dwordx4 v[56:59], v206, s[52:53] offset:64
	global_load_dwordx4 v[60:63], v206, s[54:55] offset:64
	global_load_dwordx4 v[64:67], v206, s[56:57] offset:64
	global_load_dwordx4 v[68:71], v206, s[58:59] offset:64
	global_load_dwordx4 v[72:75], v206, s[42:43] offset:128
	global_load_dwordx4 v[76:79], v206, s[44:45] offset:128
	global_load_dwordx4 v[80:83], v206, s[46:47] offset:128
	global_load_dwordx4 v[84:87], v206, s[48:49] offset:128
	global_load_dwordx4 v[88:91], v206, s[50:51] offset:128
	global_load_dwordx4 v[92:95], v206, s[52:53] offset:128
	global_load_dwordx4 v[96:99], v206, s[54:55] offset:128
	global_load_dwordx4 v[100:103], v206, s[56:57] offset:128
	global_load_dwordx4 v[104:107], v206, s[58:59] offset:128
	s_waitcnt vmcnt(18)
	v_mfma_f32_16x16x32_bf16 v[108:111], v[16:19], v[0:3], v[108:111]
	v_mfma_f32_16x16x32_bf16 v[112:115], v[20:23], v[0:3], v[112:115]
	v_mfma_f32_16x16x32_bf16 v[116:119], v[24:27], v[0:3], v[116:119]
	v_mfma_f32_16x16x32_bf16 v[120:123], v[28:31], v[0:3], v[120:123]
	v_mfma_f32_16x16x32_bf16 v[124:127], v[32:35], v[0:3], v[124:127]
	v_mfma_f32_16x16x32_bf16 v[146:149], v[16:19], v[4:7], v[146:149]
	v_mfma_f32_16x16x32_bf16 v[150:153], v[20:23], v[4:7], v[150:153]
	v_mfma_f32_16x16x32_bf16 v[154:157], v[24:27], v[4:7], v[154:157]
	v_mfma_f32_16x16x32_bf16 v[158:161], v[28:31], v[4:7], v[158:161]
	v_mfma_f32_16x16x32_bf16 v[162:165], v[32:35], v[4:7], v[162:165]
	v_mfma_f32_16x16x32_bf16 v[166:169], v[16:19], v[8:11], v[166:169]
	v_mfma_f32_16x16x32_bf16 v[170:173], v[20:23], v[8:11], v[170:173]
	v_mfma_f32_16x16x32_bf16 v[174:177], v[24:27], v[8:11], v[174:177]
	v_mfma_f32_16x16x32_bf16 v[178:181], v[28:31], v[8:11], v[178:181]
	v_mfma_f32_16x16x32_bf16 v[212:215], v[32:35], v[8:11], v[212:215]
	v_mfma_f32_16x16x32_bf16 v[216:219], v[16:19], v[12:15], v[216:219]
	v_mfma_f32_16x16x32_bf16 v[220:223], v[20:23], v[12:15], v[220:223]
	v_mfma_f32_16x16x32_bf16 v[224:227], v[24:27], v[12:15], v[224:227]
	v_mfma_f32_16x16x32_bf16 v[228:231], v[28:31], v[12:15], v[228:231]
	v_mfma_f32_16x16x32_bf16 v[232:235], v[32:35], v[12:15], v[232:235]
	global_load_dwordx4 v[0:3], v206, s[42:43] offset:192
	global_load_dwordx4 v[4:7], v206, s[44:45] offset:192
	global_load_dwordx4 v[8:11], v206, s[46:47] offset:192
	global_load_dwordx4 v[12:15], v206, s[48:49] offset:192
	global_load_dwordx4 v[16:19], v206, s[50:51] offset:192
	global_load_dwordx4 v[20:23], v206, s[52:53] offset:192
	global_load_dwordx4 v[24:27], v206, s[54:55] offset:192
	global_load_dwordx4 v[28:31], v206, s[56:57] offset:192
	global_load_dwordx4 v[32:35], v206, s[58:59] offset:192
	s_waitcnt vmcnt(18)
	v_mfma_f32_16x16x32_bf16 v[108:111], v[52:55], v[36:39], v[108:111]
	v_mfma_f32_16x16x32_bf16 v[112:115], v[56:59], v[36:39], v[112:115]
	v_mfma_f32_16x16x32_bf16 v[116:119], v[60:63], v[36:39], v[116:119]
	v_mfma_f32_16x16x32_bf16 v[120:123], v[64:67], v[36:39], v[120:123]
	v_mfma_f32_16x16x32_bf16 v[124:127], v[68:71], v[36:39], v[124:127]
	v_mfma_f32_16x16x32_bf16 v[146:149], v[52:55], v[40:43], v[146:149]
	v_mfma_f32_16x16x32_bf16 v[150:153], v[56:59], v[40:43], v[150:153]
	v_mfma_f32_16x16x32_bf16 v[154:157], v[60:63], v[40:43], v[154:157]
	v_mfma_f32_16x16x32_bf16 v[158:161], v[64:67], v[40:43], v[158:161]
	v_mfma_f32_16x16x32_bf16 v[162:165], v[68:71], v[40:43], v[162:165]
	v_mfma_f32_16x16x32_bf16 v[166:169], v[52:55], v[44:47], v[166:169]
	v_mfma_f32_16x16x32_bf16 v[170:173], v[56:59], v[44:47], v[170:173]
	v_mfma_f32_16x16x32_bf16 v[174:177], v[60:63], v[44:47], v[174:177]
	v_mfma_f32_16x16x32_bf16 v[178:181], v[64:67], v[44:47], v[178:181]
	v_mfma_f32_16x16x32_bf16 v[212:215], v[68:71], v[44:47], v[212:215]
	v_mfma_f32_16x16x32_bf16 v[216:219], v[52:55], v[48:51], v[216:219]
	v_mfma_f32_16x16x32_bf16 v[220:223], v[56:59], v[48:51], v[220:223]
	v_mfma_f32_16x16x32_bf16 v[224:227], v[60:63], v[48:51], v[224:227]
	v_mfma_f32_16x16x32_bf16 v[228:231], v[64:67], v[48:51], v[228:231]
	v_mfma_f32_16x16x32_bf16 v[232:235], v[68:71], v[48:51], v[232:235]
	global_load_dwordx4 v[36:39], v206, s[42:43] offset:256
	global_load_dwordx4 v[40:43], v206, s[44:45] offset:256
	global_load_dwordx4 v[44:47], v206, s[46:47] offset:256
	global_load_dwordx4 v[48:51], v206, s[48:49] offset:256
	global_load_dwordx4 v[52:55], v206, s[50:51] offset:256
	global_load_dwordx4 v[56:59], v206, s[52:53] offset:256
	global_load_dwordx4 v[60:63], v206, s[54:55] offset:256
	global_load_dwordx4 v[64:67], v206, s[56:57] offset:256
	global_load_dwordx4 v[68:71], v206, s[58:59] offset:256
	s_waitcnt vmcnt(18)
	v_mfma_f32_16x16x32_bf16 v[108:111], v[88:91], v[72:75], v[108:111]
	v_mfma_f32_16x16x32_bf16 v[112:115], v[92:95], v[72:75], v[112:115]
	v_mfma_f32_16x16x32_bf16 v[116:119], v[96:99], v[72:75], v[116:119]
	v_mfma_f32_16x16x32_bf16 v[120:123], v[100:103], v[72:75], v[120:123]
	v_mfma_f32_16x16x32_bf16 v[124:127], v[104:107], v[72:75], v[124:127]
	v_mfma_f32_16x16x32_bf16 v[146:149], v[88:91], v[76:79], v[146:149]
	v_mfma_f32_16x16x32_bf16 v[150:153], v[92:95], v[76:79], v[150:153]
	v_mfma_f32_16x16x32_bf16 v[154:157], v[96:99], v[76:79], v[154:157]
	v_mfma_f32_16x16x32_bf16 v[158:161], v[100:103], v[76:79], v[158:161]
	v_mfma_f32_16x16x32_bf16 v[162:165], v[104:107], v[76:79], v[162:165]
	v_mfma_f32_16x16x32_bf16 v[166:169], v[88:91], v[80:83], v[166:169]
	v_mfma_f32_16x16x32_bf16 v[170:173], v[92:95], v[80:83], v[170:173]
	v_mfma_f32_16x16x32_bf16 v[174:177], v[96:99], v[80:83], v[174:177]
	v_mfma_f32_16x16x32_bf16 v[178:181], v[100:103], v[80:83], v[178:181]
	v_mfma_f32_16x16x32_bf16 v[212:215], v[104:107], v[80:83], v[212:215]
	v_mfma_f32_16x16x32_bf16 v[216:219], v[88:91], v[84:87], v[216:219]
	v_mfma_f32_16x16x32_bf16 v[220:223], v[92:95], v[84:87], v[220:223]
	v_mfma_f32_16x16x32_bf16 v[224:227], v[96:99], v[84:87], v[224:227]
	v_mfma_f32_16x16x32_bf16 v[228:231], v[100:103], v[84:87], v[228:231]
	v_mfma_f32_16x16x32_bf16 v[232:235], v[104:107], v[84:87], v[232:235]
	global_load_dwordx4 v[72:75], v206, s[42:43] offset:320
	global_load_dwordx4 v[76:79], v206, s[44:45] offset:320
	global_load_dwordx4 v[80:83], v206, s[46:47] offset:320
	global_load_dwordx4 v[84:87], v206, s[48:49] offset:320
	global_load_dwordx4 v[88:91], v206, s[50:51] offset:320
	global_load_dwordx4 v[92:95], v206, s[52:53] offset:320
	global_load_dwordx4 v[96:99], v206, s[54:55] offset:320
	global_load_dwordx4 v[100:103], v206, s[56:57] offset:320
	global_load_dwordx4 v[104:107], v206, s[58:59] offset:320
	s_waitcnt vmcnt(18)
	v_mfma_f32_16x16x32_bf16 v[108:111], v[16:19], v[0:3], v[108:111]
	v_mfma_f32_16x16x32_bf16 v[112:115], v[20:23], v[0:3], v[112:115]
	v_mfma_f32_16x16x32_bf16 v[116:119], v[24:27], v[0:3], v[116:119]
	v_mfma_f32_16x16x32_bf16 v[120:123], v[28:31], v[0:3], v[120:123]
	v_mfma_f32_16x16x32_bf16 v[124:127], v[32:35], v[0:3], v[124:127]
	v_mfma_f32_16x16x32_bf16 v[146:149], v[16:19], v[4:7], v[146:149]
	v_mfma_f32_16x16x32_bf16 v[150:153], v[20:23], v[4:7], v[150:153]
	v_mfma_f32_16x16x32_bf16 v[154:157], v[24:27], v[4:7], v[154:157]
	v_mfma_f32_16x16x32_bf16 v[158:161], v[28:31], v[4:7], v[158:161]
	v_mfma_f32_16x16x32_bf16 v[162:165], v[32:35], v[4:7], v[162:165]
	v_mfma_f32_16x16x32_bf16 v[166:169], v[16:19], v[8:11], v[166:169]
	v_mfma_f32_16x16x32_bf16 v[170:173], v[20:23], v[8:11], v[170:173]
	v_mfma_f32_16x16x32_bf16 v[174:177], v[24:27], v[8:11], v[174:177]
	v_mfma_f32_16x16x32_bf16 v[178:181], v[28:31], v[8:11], v[178:181]
	v_mfma_f32_16x16x32_bf16 v[212:215], v[32:35], v[8:11], v[212:215]
	v_mfma_f32_16x16x32_bf16 v[216:219], v[16:19], v[12:15], v[216:219]
	v_mfma_f32_16x16x32_bf16 v[220:223], v[20:23], v[12:15], v[220:223]
	v_mfma_f32_16x16x32_bf16 v[224:227], v[24:27], v[12:15], v[224:227]
	v_mfma_f32_16x16x32_bf16 v[228:231], v[28:31], v[12:15], v[228:231]
	v_mfma_f32_16x16x32_bf16 v[232:235], v[32:35], v[12:15], v[232:235]
	global_load_dwordx4 v[0:3], v206, s[42:43] offset:384
	global_load_dwordx4 v[4:7], v206, s[44:45] offset:384
	global_load_dwordx4 v[8:11], v206, s[46:47] offset:384
	global_load_dwordx4 v[12:15], v206, s[48:49] offset:384
	global_load_dwordx4 v[16:19], v206, s[50:51] offset:384
	global_load_dwordx4 v[20:23], v206, s[52:53] offset:384
	global_load_dwordx4 v[24:27], v206, s[54:55] offset:384
	global_load_dwordx4 v[28:31], v206, s[56:57] offset:384
	global_load_dwordx4 v[32:35], v206, s[58:59] offset:384
	s_waitcnt vmcnt(18)
	v_mfma_f32_16x16x32_bf16 v[108:111], v[52:55], v[36:39], v[108:111]
	v_mfma_f32_16x16x32_bf16 v[112:115], v[56:59], v[36:39], v[112:115]
	v_mfma_f32_16x16x32_bf16 v[116:119], v[60:63], v[36:39], v[116:119]
	v_mfma_f32_16x16x32_bf16 v[120:123], v[64:67], v[36:39], v[120:123]
	v_mfma_f32_16x16x32_bf16 v[124:127], v[68:71], v[36:39], v[124:127]
	v_mfma_f32_16x16x32_bf16 v[146:149], v[52:55], v[40:43], v[146:149]
	v_mfma_f32_16x16x32_bf16 v[150:153], v[56:59], v[40:43], v[150:153]
	v_mfma_f32_16x16x32_bf16 v[154:157], v[60:63], v[40:43], v[154:157]
	v_mfma_f32_16x16x32_bf16 v[158:161], v[64:67], v[40:43], v[158:161]
	v_mfma_f32_16x16x32_bf16 v[162:165], v[68:71], v[40:43], v[162:165]
	v_mfma_f32_16x16x32_bf16 v[166:169], v[52:55], v[44:47], v[166:169]
	v_mfma_f32_16x16x32_bf16 v[170:173], v[56:59], v[44:47], v[170:173]
	v_mfma_f32_16x16x32_bf16 v[174:177], v[60:63], v[44:47], v[174:177]
	v_mfma_f32_16x16x32_bf16 v[178:181], v[64:67], v[44:47], v[178:181]
	v_mfma_f32_16x16x32_bf16 v[212:215], v[68:71], v[44:47], v[212:215]
	v_mfma_f32_16x16x32_bf16 v[216:219], v[52:55], v[48:51], v[216:219]
	v_mfma_f32_16x16x32_bf16 v[220:223], v[56:59], v[48:51], v[220:223]
	v_mfma_f32_16x16x32_bf16 v[224:227], v[60:63], v[48:51], v[224:227]
	v_mfma_f32_16x16x32_bf16 v[228:231], v[64:67], v[48:51], v[228:231]
	v_mfma_f32_16x16x32_bf16 v[232:235], v[68:71], v[48:51], v[232:235]
	global_load_dwordx4 v[36:39], v206, s[42:43] offset:448
	global_load_dwordx4 v[40:43], v206, s[44:45] offset:448
	global_load_dwordx4 v[44:47], v206, s[46:47] offset:448
	global_load_dwordx4 v[48:51], v206, s[48:49] offset:448
	global_load_dwordx4 v[52:55], v206, s[50:51] offset:448
	global_load_dwordx4 v[56:59], v206, s[52:53] offset:448
	global_load_dwordx4 v[60:63], v206, s[54:55] offset:448
	global_load_dwordx4 v[64:67], v206, s[56:57] offset:448
	global_load_dwordx4 v[68:71], v206, s[58:59] offset:448
	s_waitcnt vmcnt(18)
	v_mfma_f32_16x16x32_bf16 v[108:111], v[88:91], v[72:75], v[108:111]
	v_mfma_f32_16x16x32_bf16 v[112:115], v[92:95], v[72:75], v[112:115]
	v_mfma_f32_16x16x32_bf16 v[116:119], v[96:99], v[72:75], v[116:119]
	v_mfma_f32_16x16x32_bf16 v[120:123], v[100:103], v[72:75], v[120:123]
	v_mfma_f32_16x16x32_bf16 v[124:127], v[104:107], v[72:75], v[124:127]
	v_mfma_f32_16x16x32_bf16 v[146:149], v[88:91], v[76:79], v[146:149]
	v_mfma_f32_16x16x32_bf16 v[150:153], v[92:95], v[76:79], v[150:153]
	v_mfma_f32_16x16x32_bf16 v[154:157], v[96:99], v[76:79], v[154:157]
	v_mfma_f32_16x16x32_bf16 v[158:161], v[100:103], v[76:79], v[158:161]
	v_mfma_f32_16x16x32_bf16 v[162:165], v[104:107], v[76:79], v[162:165]
	v_mfma_f32_16x16x32_bf16 v[166:169], v[88:91], v[80:83], v[166:169]
	v_mfma_f32_16x16x32_bf16 v[170:173], v[92:95], v[80:83], v[170:173]
	v_mfma_f32_16x16x32_bf16 v[174:177], v[96:99], v[80:83], v[174:177]
	v_mfma_f32_16x16x32_bf16 v[178:181], v[100:103], v[80:83], v[178:181]
	v_mfma_f32_16x16x32_bf16 v[212:215], v[104:107], v[80:83], v[212:215]
	v_mfma_f32_16x16x32_bf16 v[216:219], v[88:91], v[84:87], v[216:219]
	v_mfma_f32_16x16x32_bf16 v[220:223], v[92:95], v[84:87], v[220:223]
	v_mfma_f32_16x16x32_bf16 v[224:227], v[96:99], v[84:87], v[224:227]
	v_mfma_f32_16x16x32_bf16 v[228:231], v[100:103], v[84:87], v[228:231]
	v_mfma_f32_16x16x32_bf16 v[232:235], v[104:107], v[84:87], v[232:235]
	s_waitcnt vmcnt(9)
	v_mfma_f32_16x16x32_bf16 v[108:111], v[16:19], v[0:3], v[108:111]
	v_mfma_f32_16x16x32_bf16 v[112:115], v[20:23], v[0:3], v[112:115]
	v_mfma_f32_16x16x32_bf16 v[116:119], v[24:27], v[0:3], v[116:119]
	v_mfma_f32_16x16x32_bf16 v[120:123], v[28:31], v[0:3], v[120:123]
	v_mfma_f32_16x16x32_bf16 v[124:127], v[32:35], v[0:3], v[124:127]
	v_mfma_f32_16x16x32_bf16 v[146:149], v[16:19], v[4:7], v[146:149]
	v_mfma_f32_16x16x32_bf16 v[150:153], v[20:23], v[4:7], v[150:153]
	v_mfma_f32_16x16x32_bf16 v[154:157], v[24:27], v[4:7], v[154:157]
	v_mfma_f32_16x16x32_bf16 v[158:161], v[28:31], v[4:7], v[158:161]
	v_mfma_f32_16x16x32_bf16 v[162:165], v[32:35], v[4:7], v[162:165]
	v_mfma_f32_16x16x32_bf16 v[166:169], v[16:19], v[8:11], v[166:169]
	v_mfma_f32_16x16x32_bf16 v[170:173], v[20:23], v[8:11], v[170:173]
	v_mfma_f32_16x16x32_bf16 v[174:177], v[24:27], v[8:11], v[174:177]
	v_mfma_f32_16x16x32_bf16 v[178:181], v[28:31], v[8:11], v[178:181]
	v_mfma_f32_16x16x32_bf16 v[212:215], v[32:35], v[8:11], v[212:215]
	v_mfma_f32_16x16x32_bf16 v[216:219], v[16:19], v[12:15], v[216:219]
	v_mfma_f32_16x16x32_bf16 v[220:223], v[20:23], v[12:15], v[220:223]
	v_mfma_f32_16x16x32_bf16 v[224:227], v[24:27], v[12:15], v[224:227]
	v_mfma_f32_16x16x32_bf16 v[228:231], v[28:31], v[12:15], v[228:231]
	v_mfma_f32_16x16x32_bf16 v[232:235], v[32:35], v[12:15], v[232:235]
	s_waitcnt vmcnt(0)
	v_mfma_f32_16x16x32_bf16 v[108:111], v[52:55], v[36:39], v[108:111]
	v_mfma_f32_16x16x32_bf16 v[112:115], v[56:59], v[36:39], v[112:115]
	v_mfma_f32_16x16x32_bf16 v[116:119], v[60:63], v[36:39], v[116:119]
	v_mfma_f32_16x16x32_bf16 v[120:123], v[64:67], v[36:39], v[120:123]
	v_mfma_f32_16x16x32_bf16 v[124:127], v[68:71], v[36:39], v[124:127]
	v_mfma_f32_16x16x32_bf16 v[146:149], v[52:55], v[40:43], v[146:149]
	v_mfma_f32_16x16x32_bf16 v[150:153], v[56:59], v[40:43], v[150:153]
	v_mfma_f32_16x16x32_bf16 v[154:157], v[60:63], v[40:43], v[154:157]
	v_mfma_f32_16x16x32_bf16 v[158:161], v[64:67], v[40:43], v[158:161]
	v_mfma_f32_16x16x32_bf16 v[162:165], v[68:71], v[40:43], v[162:165]
	v_mfma_f32_16x16x32_bf16 v[166:169], v[52:55], v[44:47], v[166:169]
	v_mfma_f32_16x16x32_bf16 v[170:173], v[56:59], v[44:47], v[170:173]
	v_mfma_f32_16x16x32_bf16 v[174:177], v[60:63], v[44:47], v[174:177]
	v_mfma_f32_16x16x32_bf16 v[178:181], v[64:67], v[44:47], v[178:181]
	v_mfma_f32_16x16x32_bf16 v[212:215], v[68:71], v[44:47], v[212:215]
	v_mfma_f32_16x16x32_bf16 v[216:219], v[52:55], v[48:51], v[216:219]
	v_mfma_f32_16x16x32_bf16 v[220:223], v[56:59], v[48:51], v[220:223]
	v_mfma_f32_16x16x32_bf16 v[224:227], v[60:63], v[48:51], v[224:227]
	v_mfma_f32_16x16x32_bf16 v[228:231], v[64:67], v[48:51], v[228:231]
	v_mfma_f32_16x16x32_bf16 v[232:235], v[68:71], v[48:51], v[232:235]
	s_nop 7
	s_nop 1
	s_cmp_lt_u32 s6, 4
	s_cbranch_scc1 .Lsk2o_a1
	ds_write_b128 v207, v[108:111] offset:0
	ds_write_b128 v207, v[112:115] offset:1024
	ds_write_b128 v207, v[116:119] offset:2048
	ds_write_b128 v207, v[120:123] offset:3072
	ds_write_b128 v207, v[124:127] offset:4096
	ds_write_b128 v207, v[146:149] offset:5120
	ds_write_b128 v207, v[150:153] offset:6144
	ds_write_b128 v207, v[154:157] offset:7168
	ds_write_b128 v207, v[158:161] offset:8192
	ds_write_b128 v207, v[162:165] offset:9216
	ds_write_b128 v207, v[166:169] offset:10240
	ds_write_b128 v207, v[170:173] offset:11264
	ds_write_b128 v207, v[174:177] offset:12288
	ds_write_b128 v207, v[178:181] offset:13312
	ds_write_b128 v207, v[212:215] offset:14336
	ds_write_b128 v207, v[216:219] offset:15360
	ds_write_b128 v207, v[220:223] offset:16384
	ds_write_b128 v207, v[224:227] offset:17408
	ds_write_b128 v207, v[228:231] offset:18432
	ds_write_b128 v207, v[232:235] offset:19456
	s_waitcnt lgkmcnt(0)
.Lsk2o_a1:
	s_barrier
	s_cmp_lt_u32 s6, 4
	s_cbranch_scc0 .Lsk2o_a2
	ds_read_b128 v[0:3], v207 offset:0
	ds_read_b128 v[4:7], v207 offset:1024
	ds_read_b128 v[8:11], v207 offset:2048
	ds_read_b128 v[12:15], v207 offset:3072
	ds_read_b128 v[16:19], v207 offset:4096
	ds_read_b128 v[20:23], v207 offset:5120
	ds_read_b128 v[24:27], v207 offset:6144
	ds_read_b128 v[28:31], v207 offset:7168
	ds_read_b128 v[32:35], v207 offset:8192
	ds_read_b128 v[36:39], v207 offset:9216
	s_waitcnt lgkmcnt(0)
	v_add_f32_e32 v108, v108, v0
	v_add_f32_e32 v109, v109, v1
	v_add_f32_e32 v110, v110, v2
	v_add_f32_e32 v111, v111, v3
	v_add_f32_e32 v112, v112, v4
	v_add_f32_e32 v113, v113, v5
	v_add_f32_e32 v114, v114, v6
	v_add_f32_e32 v115, v115, v7
	v_add_f32_e32 v116, v116, v8
	v_add_f32_e32 v117, v117, v9
	v_add_f32_e32 v118, v118, v10
	v_add_f32_e32 v119, v119, v11
	v_add_f32_e32 v120, v120, v12
	v_add_f32_e32 v121, v121, v13
	v_add_f32_e32 v122, v122, v14
	v_add_f32_e32 v123, v123, v15
	v_add_f32_e32 v124, v124, v16
	v_add_f32_e32 v125, v125, v17
	v_add_f32_e32 v126, v126, v18
	v_add_f32_e32 v127, v127, v19
	v_add_f32_e32 v146, v146, v20
	v_add_f32_e32 v147, v147, v21
	v_add_f32_e32 v148, v148, v22
	v_add_f32_e32 v149, v149, v23
	v_add_f32_e32 v150, v150, v24
	v_add_f32_e32 v151, v151, v25
	v_add_f32_e32 v152, v152, v26
	v_add_f32_e32 v153, v153, v27
	v_add_f32_e32 v154, v154, v28
	v_add_f32_e32 v155, v155, v29
	v_add_f32_e32 v156, v156, v30
	v_add_f32_e32 v157, v157, v31
	v_add_f32_e32 v158, v158, v32
	v_add_f32_e32 v159, v159, v33
	v_add_f32_e32 v160, v160, v34
	v_add_f32_e32 v161, v161, v35
	v_add_f32_e32 v162, v162, v36
	v_add_f32_e32 v163, v163, v37
	v_add_f32_e32 v164, v164, v38
	v_add_f32_e32 v165, v165, v39
	ds_read_b128 v[0:3], v207 offset:10240
	ds_read_b128 v[4:7], v207 offset:11264
	ds_read_b128 v[8:11], v207 offset:12288
	ds_read_b128 v[12:15], v207 offset:13312
	ds_read_b128 v[16:19], v207 offset:14336
	ds_read_b128 v[20:23], v207 offset:15360
	ds_read_b128 v[24:27], v207 offset:16384
	ds_read_b128 v[28:31], v207 offset:17408
	ds_read_b128 v[32:35], v207 offset:18432
	ds_read_b128 v[36:39], v207 offset:19456
	s_waitcnt lgkmcnt(0)
	v_add_f32_e32 v166, v166, v0
	v_add_f32_e32 v167, v167, v1
	v_add_f32_e32 v168, v168, v2
	v_add_f32_e32 v169, v169, v3
	v_add_f32_e32 v170, v170, v4
	v_add_f32_e32 v171, v171, v5
	v_add_f32_e32 v172, v172, v6
	v_add_f32_e32 v173, v173, v7
	v_add_f32_e32 v174, v174, v8
	v_add_f32_e32 v175, v175, v9
	v_add_f32_e32 v176, v176, v10
	v_add_f32_e32 v177, v177, v11
	v_add_f32_e32 v178, v178, v12
	v_add_f32_e32 v179, v179, v13
	v_add_f32_e32 v180, v180, v14
	v_add_f32_e32 v181, v181, v15
	v_add_f32_e32 v212, v212, v16
	v_add_f32_e32 v213, v213, v17
	v_add_f32_e32 v214, v214, v18
	v_add_f32_e32 v215, v215, v19
	v_add_f32_e32 v216, v216, v20
	v_add_f32_e32 v217, v217, v21
	v_add_f32_e32 v218, v218, v22
	v_add_f32_e32 v219, v219, v23
	v_add_f32_e32 v220, v220, v24
	v_add_f32_e32 v221, v221, v25
	v_add_f32_e32 v222, v222, v26
	v_add_f32_e32 v223, v223, v27
	v_add_f32_e32 v224, v224, v28
	v_add_f32_e32 v225, v225, v29
	v_add_f32_e32 v226, v226, v30
	v_add_f32_e32 v227, v227, v31
	v_add_f32_e32 v228, v228, v32
	v_add_f32_e32 v229, v229, v33
	v_add_f32_e32 v230, v230, v34
	v_add_f32_e32 v231, v231, v35
	v_add_f32_e32 v232, v232, v36
	v_add_f32_e32 v233, v233, v37
	v_add_f32_e32 v234, v234, v38
	v_add_f32_e32 v235, v235, v39
.Lsk2o_a2:
	s_barrier
	s_cmp_lt_u32 s6, 4
	s_cbranch_scc0 .Lsk2o_b1
	s_cmp_lt_u32 s6, 2
	s_cbranch_scc1 .Lsk2o_b1
	ds_write_b128 v207, v[108:111] offset:0
	ds_write_b128 v207, v[112:115] offset:1024
	ds_write_b128 v207, v[116:119] offset:2048
	ds_write_b128 v207, v[120:123] offset:3072
	ds_write_b128 v207, v[124:127] offset:4096
	ds_write_b128 v207, v[146:149] offset:5120
	ds_write_b128 v207, v[150:153] offset:6144
	ds_write_b128 v207, v[154:157] offset:7168
	ds_write_b128 v207, v[158:161] offset:8192
	ds_write_b128 v207, v[162:165] offset:9216
	ds_write_b128 v207, v[166:169] offset:10240
	ds_write_b128 v207, v[170:173] offset:11264
	ds_write_b128 v207, v[174:177] offset:12288
	ds_write_b128 v207, v[178:181] offset:13312
	ds_write_b128 v207, v[212:215] offset:14336
	ds_write_b128 v207, v[216:219] offset:15360
	ds_write_b128 v207, v[220:223] offset:16384
	ds_write_b128 v207, v[224:227] offset:17408
	ds_write_b128 v207, v[228:231] offset:18432
	ds_write_b128 v207, v[232:235] offset:19456
	s_waitcnt lgkmcnt(0)
.Lsk2o_b1:
	s_barrier
	s_cmp_lt_u32 s6, 2
	s_cbranch_scc0 .Lsk2o_b2
	v_add_u32_e32 v207, 0xa000, v207
	ds_read_b128 v[0:3], v207 offset:0
	ds_read_b128 v[4:7], v207 offset:1024
	ds_read_b128 v[8:11], v207 offset:2048
	ds_read_b128 v[12:15], v207 offset:3072
	ds_read_b128 v[16:19], v207 offset:4096
	ds_read_b128 v[20:23], v207 offset:5120
	ds_read_b128 v[24:27], v207 offset:6144
	ds_read_b128 v[28:31], v207 offset:7168
	ds_read_b128 v[32:35], v207 offset:8192
	ds_read_b128 v[36:39], v207 offset:9216
	s_waitcnt lgkmcnt(0)
	v_add_f32_e32 v108, v108, v0
	v_add_f32_e32 v109, v109, v1
	v_add_f32_e32 v110, v110, v2
	v_add_f32_e32 v111, v111, v3
	v_add_f32_e32 v112, v112, v4
	v_add_f32_e32 v113, v113, v5
	v_add_f32_e32 v114, v114, v6
	v_add_f32_e32 v115, v115, v7
	v_add_f32_e32 v116, v116, v8
	v_add_f32_e32 v117, v117, v9
	v_add_f32_e32 v118, v118, v10
	v_add_f32_e32 v119, v119, v11
	v_add_f32_e32 v120, v120, v12
	v_add_f32_e32 v121, v121, v13
	v_add_f32_e32 v122, v122, v14
	v_add_f32_e32 v123, v123, v15
	v_add_f32_e32 v124, v124, v16
	v_add_f32_e32 v125, v125, v17
	v_add_f32_e32 v126, v126, v18
	v_add_f32_e32 v127, v127, v19
	v_add_f32_e32 v146, v146, v20
	v_add_f32_e32 v147, v147, v21
	v_add_f32_e32 v148, v148, v22
	v_add_f32_e32 v149, v149, v23
	v_add_f32_e32 v150, v150, v24
	v_add_f32_e32 v151, v151, v25
	v_add_f32_e32 v152, v152, v26
	v_add_f32_e32 v153, v153, v27
	v_add_f32_e32 v154, v154, v28
	v_add_f32_e32 v155, v155, v29
	v_add_f32_e32 v156, v156, v30
	v_add_f32_e32 v157, v157, v31
	v_add_f32_e32 v158, v158, v32
	v_add_f32_e32 v159, v159, v33
	v_add_f32_e32 v160, v160, v34
	v_add_f32_e32 v161, v161, v35
	v_add_f32_e32 v162, v162, v36
	v_add_f32_e32 v163, v163, v37
	v_add_f32_e32 v164, v164, v38
	v_add_f32_e32 v165, v165, v39
	ds_read_b128 v[0:3], v207 offset:10240
	ds_read_b128 v[4:7], v207 offset:11264
	ds_read_b128 v[8:11], v207 offset:12288
	ds_read_b128 v[12:15], v207 offset:13312
	ds_read_b128 v[16:19], v207 offset:14336
	ds_read_b128 v[20:23], v207 offset:15360
	ds_read_b128 v[24:27], v207 offset:16384
	ds_read_b128 v[28:31], v207 offset:17408
	ds_read_b128 v[32:35], v207 offset:18432
	ds_read_b128 v[36:39], v207 offset:19456
	s_waitcnt lgkmcnt(0)
	v_add_f32_e32 v166, v166, v0
	v_add_f32_e32 v167, v167, v1
	v_add_f32_e32 v168, v168, v2
	v_add_f32_e32 v169, v169, v3
	v_add_f32_e32 v170, v170, v4
	v_add_f32_e32 v171, v171, v5
	v_add_f32_e32 v172, v172, v6
	v_add_f32_e32 v173, v173, v7
	v_add_f32_e32 v174, v174, v8
	v_add_f32_e32 v175, v175, v9
	v_add_f32_e32 v176, v176, v10
	v_add_f32_e32 v177, v177, v11
	v_add_f32_e32 v178, v178, v12
	v_add_f32_e32 v179, v179, v13
	v_add_f32_e32 v180, v180, v14
	v_add_f32_e32 v181, v181, v15
	v_add_f32_e32 v212, v212, v16
	v_add_f32_e32 v213, v213, v17
	v_add_f32_e32 v214, v214, v18
	v_add_f32_e32 v215, v215, v19
	v_add_f32_e32 v216, v216, v20
	v_add_f32_e32 v217, v217, v21
	v_add_f32_e32 v218, v218, v22
	v_add_f32_e32 v219, v219, v23
	v_add_f32_e32 v220, v220, v24
	v_add_f32_e32 v221, v221, v25
	v_add_f32_e32 v222, v222, v26
	v_add_f32_e32 v223, v223, v27
	v_add_f32_e32 v224, v224, v28
	v_add_f32_e32 v225, v225, v29
	v_add_f32_e32 v226, v226, v30
	v_add_f32_e32 v227, v227, v31
	v_add_f32_e32 v228, v228, v32
	v_add_f32_e32 v229, v229, v33
	v_add_f32_e32 v230, v230, v34
	v_add_f32_e32 v231, v231, v35
	v_add_f32_e32 v232, v232, v36
	v_add_f32_e32 v233, v233, v37
	v_add_f32_e32 v234, v234, v38
	v_add_f32_e32 v235, v235, v39
	v_add_u32_e32 v207, 0xffff6000, v207
.Lsk2o_b2:
	s_barrier
	s_cmp_eq_u32 s6, 1
	s_cbranch_scc0 .Lsk2o_c1
	ds_write_b128 v207, v[108:111] offset:0
	ds_write_b128 v207, v[112:115] offset:1024
	ds_write_b128 v207, v[116:119] offset:2048
	ds_write_b128 v207, v[120:123] offset:3072
	ds_write_b128 v207, v[124:127] offset:4096
	ds_write_b128 v207, v[146:149] offset:5120
	ds_write_b128 v207, v[150:153] offset:6144
	ds_write_b128 v207, v[154:157] offset:7168
	ds_write_b128 v207, v[158:161] offset:8192
	ds_write_b128 v207, v[162:165] offset:9216
	ds_write_b128 v207, v[166:169] offset:10240
	ds_write_b128 v207, v[170:173] offset:11264
	ds_write_b128 v207, v[174:177] offset:12288
	ds_write_b128 v207, v[178:181] offset:13312
	ds_write_b128 v207, v[212:215] offset:14336
	ds_write_b128 v207, v[216:219] offset:15360
	ds_write_b128 v207, v[220:223] offset:16384
	ds_write_b128 v207, v[224:227] offset:17408
	ds_write_b128 v207, v[228:231] offset:18432
	ds_write_b128 v207, v[232:235] offset:19456
	s_waitcnt lgkmcnt(0)
.Lsk2o_c1:
	s_barrier
	s_cmp_eq_u32 s6, 0
	s_cbranch_scc0 .Lsk2o_c2
	v_add_u32_e32 v207, 0x5000, v207
	ds_read_b128 v[0:3], v207 offset:0
	ds_read_b128 v[4:7], v207 offset:1024
	ds_read_b128 v[8:11], v207 offset:2048
	ds_read_b128 v[12:15], v207 offset:3072
	ds_read_b128 v[16:19], v207 offset:4096
	ds_read_b128 v[20:23], v207 offset:5120
	ds_read_b128 v[24:27], v207 offset:6144
	ds_read_b128 v[28:31], v207 offset:7168
	ds_read_b128 v[32:35], v207 offset:8192
	ds_read_b128 v[36:39], v207 offset:9216
	s_waitcnt lgkmcnt(0)
	v_add_f32_e32 v108, v108, v0
	v_add_f32_e32 v109, v109, v1
	v_add_f32_e32 v110, v110, v2
	v_add_f32_e32 v111, v111, v3
	v_add_f32_e32 v112, v112, v4
	v_add_f32_e32 v113, v113, v5
	v_add_f32_e32 v114, v114, v6
	v_add_f32_e32 v115, v115, v7
	v_add_f32_e32 v116, v116, v8
	v_add_f32_e32 v117, v117, v9
	v_add_f32_e32 v118, v118, v10
	v_add_f32_e32 v119, v119, v11
	v_add_f32_e32 v120, v120, v12
	v_add_f32_e32 v121, v121, v13
	v_add_f32_e32 v122, v122, v14
	v_add_f32_e32 v123, v123, v15
	v_add_f32_e32 v124, v124, v16
	v_add_f32_e32 v125, v125, v17
	v_add_f32_e32 v126, v126, v18
	v_add_f32_e32 v127, v127, v19
	v_add_f32_e32 v146, v146, v20
	v_add_f32_e32 v147, v147, v21
	v_add_f32_e32 v148, v148, v22
	v_add_f32_e32 v149, v149, v23
	v_add_f32_e32 v150, v150, v24
	v_add_f32_e32 v151, v151, v25
	v_add_f32_e32 v152, v152, v26
	v_add_f32_e32 v153, v153, v27
	v_add_f32_e32 v154, v154, v28
	v_add_f32_e32 v155, v155, v29
	v_add_f32_e32 v156, v156, v30
	v_add_f32_e32 v157, v157, v31
	v_add_f32_e32 v158, v158, v32
	v_add_f32_e32 v159, v159, v33
	v_add_f32_e32 v160, v160, v34
	v_add_f32_e32 v161, v161, v35
	v_add_f32_e32 v162, v162, v36
	v_add_f32_e32 v163, v163, v37
	v_add_f32_e32 v164, v164, v38
	v_add_f32_e32 v165, v165, v39
	ds_read_b128 v[0:3], v207 offset:10240
	ds_read_b128 v[4:7], v207 offset:11264
	ds_read_b128 v[8:11], v207 offset:12288
	ds_read_b128 v[12:15], v207 offset:13312
	ds_read_b128 v[16:19], v207 offset:14336
	ds_read_b128 v[20:23], v207 offset:15360
	ds_read_b128 v[24:27], v207 offset:16384
	ds_read_b128 v[28:31], v207 offset:17408
	ds_read_b128 v[32:35], v207 offset:18432
	ds_read_b128 v[36:39], v207 offset:19456
	s_waitcnt lgkmcnt(0)
	v_add_f32_e32 v166, v166, v0
	v_add_f32_e32 v167, v167, v1
	v_add_f32_e32 v168, v168, v2
	v_add_f32_e32 v169, v169, v3
	v_add_f32_e32 v170, v170, v4
	v_add_f32_e32 v171, v171, v5
	v_add_f32_e32 v172, v172, v6
	v_add_f32_e32 v173, v173, v7
	v_add_f32_e32 v174, v174, v8
	v_add_f32_e32 v175, v175, v9
	v_add_f32_e32 v176, v176, v10
	v_add_f32_e32 v177, v177, v11
	v_add_f32_e32 v178, v178, v12
	v_add_f32_e32 v179, v179, v13
	v_add_f32_e32 v180, v180, v14
	v_add_f32_e32 v181, v181, v15
	v_add_f32_e32 v212, v212, v16
	v_add_f32_e32 v213, v213, v17
	v_add_f32_e32 v214, v214, v18
	v_add_f32_e32 v215, v215, v19
	v_add_f32_e32 v216, v216, v20
	v_add_f32_e32 v217, v217, v21
	v_add_f32_e32 v218, v218, v22
	v_add_f32_e32 v219, v219, v23
	v_add_f32_e32 v220, v220, v24
	v_add_f32_e32 v221, v221, v25
	v_add_f32_e32 v222, v222, v26
	v_add_f32_e32 v223, v223, v27
	v_add_f32_e32 v224, v224, v28
	v_add_f32_e32 v225, v225, v29
	v_add_f32_e32 v226, v226, v30
	v_add_f32_e32 v227, v227, v31
	v_add_f32_e32 v228, v228, v32
	v_add_f32_e32 v229, v229, v33
	v_add_f32_e32 v230, v230, v34
	v_add_f32_e32 v231, v231, v35
	v_add_f32_e32 v232, v232, v36
	v_add_f32_e32 v233, v233, v37
	v_add_f32_e32 v234, v234, v38
	v_add_f32_e32 v235, v235, v39
	v_add_u32_e32 v207, 0xffffb000, v207
	s_lshl_b32 s60, s64, 15
	s_add_u32 s60, s60, 0x31200000
	s_add_u32 s60, s8, s60
	s_addc_u32 s61, s9, 0
	global_store_dwordx4 v208, v[108:111], s[60:61]
	global_store_dwordx4 v208, v[112:115], s[60:61] offset:64
	global_store_dwordx4 v208, v[116:119], s[60:61] offset:128
	global_store_dwordx4 v208, v[120:123], s[60:61] offset:192
	global_store_dwordx4 v208, v[124:127], s[60:61] offset:256
	s_add_u32 s60, s60, 0x2000
	s_addc_u32 s61, s61, 0
	global_store_dwordx4 v208, v[146:149], s[60:61]
	global_store_dwordx4 v208, v[150:153], s[60:61] offset:64
	global_store_dwordx4 v208, v[154:157], s[60:61] offset:128
	global_store_dwordx4 v208, v[158:161], s[60:61] offset:192
	global_store_dwordx4 v208, v[162:165], s[60:61] offset:256
	s_add_u32 s60, s60, 0x2000
	s_addc_u32 s61, s61, 0
	global_store_dwordx4 v208, v[166:169], s[60:61]
	global_store_dwordx4 v208, v[170:173], s[60:61] offset:64
	global_store_dwordx4 v208, v[174:177], s[60:61] offset:128
	global_store_dwordx4 v208, v[178:181], s[60:61] offset:192
	global_store_dwordx4 v208, v[212:215], s[60:61] offset:256
	s_add_u32 s60, s60, 0x2000
	s_addc_u32 s61, s61, 0
	global_store_dwordx4 v208, v[216:219], s[60:61]
	global_store_dwordx4 v208, v[220:223], s[60:61] offset:64
	global_store_dwordx4 v208, v[224:227], s[60:61] offset:128
	global_store_dwordx4 v208, v[228:231], s[60:61] offset:192
	global_store_dwordx4 v208, v[232:235], s[60:61] offset:256

.Lsk2_next:
	s_add_i32 s64, s64, s63
	s_cmpk_lt_u32 s64, 0x100
	s_cbranch_scc1 .Lsk2_loop
